# ssd_out intra-chunk loop: the 32 exec-masked decay-mask blocks per iteration (each its own ds_read_b32, lgkmcnt(0), exp) replaced by 8 ds_read_b128 up front and branch-free sub/mul/exp/mul plus v_cndm
# speedup vs baseline: 1.0141x; 1.0007x over previous
.LBB0_588:
	v_add_u32_e32 v160, s12, v83
	v_xor_b32_e32 v66, v160, v117
	v_lshl_add_u32 v161, v66, 4, v126
	v_add_u32_e32 v66, v161, v88
	ds_read_b64_tr_b16 v[66:67], v66
	v_xor_b32_e32 v68, v160, v118
	v_lshl_add_u32 v68, v68, 4, v128
	ds_read_b64_tr_b16 v[68:69], v68
	ds_read_b64_tr_b16 v[70:71], v89
	ds_read_b64_tr_b16 v[72:73], v90
	v_add_u32_e32 v152, v161, v91
	ds_read_b64_tr_b16 v[152:153], v152
	v_xor_b32_e32 v154, v160, v119
	v_lshl_add_u32 v154, v154, 4, v129
	ds_read_b64_tr_b16 v[154:155], v154
	ds_read_b64_tr_b16 v[156:157], v92
	ds_read_b64_tr_b16 v[158:159], v93
	s_waitcnt lgkmcnt(4)
	v_mfma_f32_32x32x16_bf16 v[66:81], v[66:69], v[70:73], 0
	v_cmp_le_i32_e32 vcc, v151, v110
	s_waitcnt lgkmcnt(0)
	v_mfma_f32_32x32x16_bf16 v[66:81], v[152:155], v[156:159], v[66:81]
	v_add_u32_e32 v152, v161, v94
	ds_read_b64_tr_b16 v[152:153], v152
	v_xor_b32_e32 v154, v160, v120
	v_lshl_add_u32 v154, v154, 4, v130
	ds_read_b64_tr_b16 v[154:155], v154
	ds_read_b64_tr_b16 v[156:157], v95
	ds_read_b64_tr_b16 v[158:159], v96
	s_waitcnt lgkmcnt(0)
	v_mfma_f32_32x32x16_bf16 v[66:81], v[152:155], v[156:159], v[66:81]
	v_add_u32_e32 v152, v161, v97
	ds_read_b64_tr_b16 v[152:153], v152
	v_xor_b32_e32 v154, v160, v121
	v_lshl_add_u32 v154, v154, 4, v131
	ds_read_b64_tr_b16 v[154:155], v154
	ds_read_b64_tr_b16 v[156:157], v98
	ds_read_b64_tr_b16 v[158:159], v99
	s_waitcnt lgkmcnt(0)
	v_mfma_f32_32x32x16_bf16 v[66:81], v[152:155], v[156:159], v[66:81]
	v_add_u32_e32 v152, v161, v100
	ds_read_b64_tr_b16 v[152:153], v152
	v_xor_b32_e32 v154, v160, v122
	v_lshl_add_u32 v154, v154, 4, v132
	ds_read_b64_tr_b16 v[154:155], v154
	ds_read_b64_tr_b16 v[156:157], v101
	ds_read_b64_tr_b16 v[158:159], v102
	s_waitcnt lgkmcnt(0)
	v_mfma_f32_32x32x16_bf16 v[66:81], v[152:155], v[156:159], v[66:81]
	v_add_u32_e32 v152, v161, v103
	ds_read_b64_tr_b16 v[152:153], v152
	v_xor_b32_e32 v154, v160, v123
	v_lshl_add_u32 v154, v154, 4, v133
	ds_read_b64_tr_b16 v[154:155], v154
	ds_read_b64_tr_b16 v[156:157], v104
	ds_read_b64_tr_b16 v[158:159], v105
	s_waitcnt lgkmcnt(0)
	v_mfma_f32_32x32x16_bf16 v[66:81], v[152:155], v[156:159], v[66:81]
	v_add_u32_e32 v152, v161, v106
	ds_read_b64_tr_b16 v[152:153], v152
	v_xor_b32_e32 v154, v160, v124
	v_lshl_add_u32 v154, v154, 4, v134
	ds_read_b64_tr_b16 v[154:155], v154
	ds_read_b64_tr_b16 v[156:157], v107
	ds_read_b64_tr_b16 v[158:159], v108
	s_waitcnt lgkmcnt(0)
	v_mfma_f32_32x32x16_bf16 v[66:81], v[152:155], v[156:159], v[66:81]
	v_add_u32_e32 v152, v161, v111
	ds_read_b64_tr_b16 v[152:153], v152
	v_xor_b32_e32 v154, v160, v125
	v_lshl_add_u32 v154, v154, 4, v135
	ds_read_b64_tr_b16 v[154:155], v154
	ds_read_b64_tr_b16 v[156:157], v113
	ds_read_b64_tr_b16 v[158:159], v114
	s_waitcnt lgkmcnt(0)
	v_mfma_f32_32x32x16_bf16 v[66:81], v[152:155], v[156:159], v[66:81]
	ds_read_b128 v[192:195], v150
	ds_read_b128 v[196:199], v150 offset:32
	ds_read_b128 v[200:203], v150 offset:64
	ds_read_b128 v[204:207], v150 offset:96
	ds_read_b128 v[212:215], v149
	ds_read_b128 v[216:219], v149 offset:32
	ds_read_b128 v[220:223], v149 offset:64
	ds_read_b128 v[224:227], v149 offset:96
	v_cmp_lt_i32_e64 s[38:39], v151, v110
	v_add_u32_e32 v152, 2, v151
	v_cmp_le_i32_e64 s[40:41], v152, v110
	v_add_u32_e32 v152, 3, v151
	v_cmp_le_i32_e64 s[42:43], v152, v110
	v_cmp_le_i32_e64 s[44:45], v151, v137
	v_cmp_le_i32_e64 s[46:47], v151, v138
	v_cmp_le_i32_e64 s[48:49], v151, v139
	v_cmp_le_i32_e64 s[50:51], v151, v140
	v_cmp_le_i32_e64 s[52:53], v151, v141
	v_cmp_le_i32_e64 s[54:55], v151, v142
	v_cmp_le_i32_e64 s[56:57], v151, v143
	v_cmp_le_i32_e64 s[58:59], v151, v144
	v_cmp_le_i32_e64 s[60:61], v151, v145
	v_cmp_le_i32_e64 s[62:63], v151, v146
	v_cmp_le_i32_e64 s[64:65], v151, v147
	v_cmp_le_i32_e64 s[66:67], v151, v148
	s_waitcnt lgkmcnt(0)
	v_sub_f32_e32 v192, v115, v192
	v_sub_f32_e32 v193, v115, v193
	v_sub_f32_e32 v194, v115, v194
	v_sub_f32_e32 v195, v115, v195
	v_sub_f32_e32 v196, v115, v196
	v_sub_f32_e32 v197, v115, v197
	v_sub_f32_e32 v198, v115, v198
	v_sub_f32_e32 v199, v115, v199
	v_sub_f32_e32 v200, v115, v200
	v_sub_f32_e32 v201, v115, v201
	v_sub_f32_e32 v202, v115, v202
	v_sub_f32_e32 v203, v115, v203
	v_sub_f32_e32 v204, v115, v204
	v_sub_f32_e32 v205, v115, v205
	v_sub_f32_e32 v206, v115, v206
	v_sub_f32_e32 v207, v115, v207
	v_mul_f32_e32 v192, 0x3fb8aa3b, v192
	v_mul_f32_e32 v193, 0x3fb8aa3b, v193
	v_mul_f32_e32 v194, 0x3fb8aa3b, v194
	v_mul_f32_e32 v195, 0x3fb8aa3b, v195
	v_mul_f32_e32 v196, 0x3fb8aa3b, v196
	v_mul_f32_e32 v197, 0x3fb8aa3b, v197
	v_mul_f32_e32 v198, 0x3fb8aa3b, v198
	v_mul_f32_e32 v199, 0x3fb8aa3b, v199
	v_mul_f32_e32 v200, 0x3fb8aa3b, v200
	v_mul_f32_e32 v201, 0x3fb8aa3b, v201
	v_mul_f32_e32 v202, 0x3fb8aa3b, v202
	v_mul_f32_e32 v203, 0x3fb8aa3b, v203
	v_mul_f32_e32 v204, 0x3fb8aa3b, v204
	v_mul_f32_e32 v205, 0x3fb8aa3b, v205
	v_mul_f32_e32 v206, 0x3fb8aa3b, v206
	v_mul_f32_e32 v207, 0x3fb8aa3b, v207
	v_exp_f32_e32 v192, v192
	v_exp_f32_e32 v193, v193
	v_exp_f32_e32 v194, v194
	v_exp_f32_e32 v195, v195
	v_exp_f32_e32 v196, v196
	v_exp_f32_e32 v197, v197
	v_exp_f32_e32 v198, v198
	v_exp_f32_e32 v199, v199
	v_exp_f32_e32 v200, v200
	v_exp_f32_e32 v201, v201
	v_exp_f32_e32 v202, v202
	v_exp_f32_e32 v203, v203
	v_exp_f32_e32 v204, v204
	v_exp_f32_e32 v205, v205
	v_exp_f32_e32 v206, v206
	v_exp_f32_e32 v207, v207
	v_mul_f32_e32 v192, v66, v192
	v_mul_f32_e32 v193, v67, v193
	v_mul_f32_e32 v194, v68, v194
	v_mul_f32_e32 v195, v69, v195
	v_mul_f32_e32 v196, v70, v196
	v_mul_f32_e32 v197, v71, v197
	v_mul_f32_e32 v198, v72, v198
	v_mul_f32_e32 v199, v73, v199
	v_mul_f32_e32 v200, v74, v200
	v_mul_f32_e32 v201, v75, v201
	v_mul_f32_e32 v202, v76, v202
	v_mul_f32_e32 v203, v77, v203
	v_mul_f32_e32 v204, v78, v204
	v_mul_f32_e32 v205, v79, v205
	v_mul_f32_e32 v206, v80, v206
	v_mul_f32_e32 v207, v81, v207
	v_cndmask_b32_e64 v155, 0, v192, vcc
	v_cndmask_b32_e64 v156, 0, v193, s[38:39]
	v_cndmask_b32_e64 v154, 0, v194, s[40:41]
	v_cndmask_b32_e64 v158, 0, v195, s[42:43]
	v_cndmask_b32_e64 v157, 0, v196, s[44:45]
	v_cndmask_b32_e64 v160, 0, v197, s[46:47]
	v_cndmask_b32_e64 v159, 0, v198, s[48:49]
	v_cndmask_b32_e64 v161, 0, v199, s[50:51]
	v_cndmask_b32_e64 v162, 0, v200, s[52:53]
	v_cndmask_b32_e64 v165, 0, v201, s[54:55]
	v_cndmask_b32_e64 v164, 0, v202, s[56:57]
	v_cndmask_b32_e64 v168, 0, v203, s[58:59]
	v_cndmask_b32_e64 v167, 0, v204, s[60:61]
	v_cndmask_b32_e64 v169, 0, v205, s[62:63]
	v_cndmask_b32_e64 v163, 0, v206, s[64:65]
	v_cndmask_b32_e64 v166, 0, v207, s[66:67]
	s_add_i32 s18, s12, 2
	v_xor_b32_e32 v152, s18, v127
	v_cvt_pk_bf16_f32 v175, v154, v158
	v_xor_b32_e32 v154, s12, v127
	s_add_i32 s18, s12, 1
	v_cvt_pk_bf16_f32 v174, v155, v156
	v_lshl_add_u32 v155, v154, 4, v84
	v_xor_b32_e32 v154, s18, v127
	v_lshl_add_u32 v154, v154, 4, v84
	v_cvt_pk_bf16_f32 v176, v157, v160
	v_add_u32_e32 v156, v155, v136
	v_add_u32_e32 v160, v154, v136
	v_cvt_pk_bf16_f32 v177, v159, v161
	ds_read2st64_b64 v[156:159], v156 offset0:16 offset1:32
	ds_read2st64_b64 v[178:181], v160 offset0:16 offset1:32
	s_add_i32 s18, s12, 3
	v_lshl_add_u32 v152, v152, 4, v84
	v_cvt_pk_bf16_f32 v170, v162, v165
	s_waitcnt lgkmcnt(1)
	v_mov_b32_e32 v186, v156
	v_mov_b32_e32 v187, v157
	s_waitcnt lgkmcnt(0)
	v_mov_b32_e32 v188, v178
	v_mov_b32_e32 v189, v179
	v_mov_b32_e32 v178, v158
	v_mov_b32_e32 v179, v159
	v_xor_b32_e32 v156, s18, v127
	v_lshl_add_u32 v156, v156, 4, v84
	v_add_u32_e32 v157, v152, v136
	ds_read2st64_b64 v[158:161], v157 offset0:16 offset1:32
	v_add_u32_e32 v157, v156, v136
	v_cvt_pk_bf16_f32 v171, v164, v168
	v_cvt_pk_bf16_f32 v173, v163, v166
	ds_read2st64_b64 v[162:165], v157 offset0:16 offset1:32
	v_mfma_f32_32x32x16_bf16 v[50:65], v[186:189], v[174:177], v[50:65]
	v_cvt_pk_bf16_f32 v172, v167, v169
	s_waitcnt lgkmcnt(1)
	v_mov_b32_e32 v166, v158
	v_mov_b32_e32 v167, v159
	s_waitcnt lgkmcnt(0)
	v_mov_b32_e32 v168, v162
	v_mov_b32_e32 v169, v163
	v_mov_b32_e32 v162, v160
	v_mov_b32_e32 v163, v161
	v_mfma_f32_32x32x16_bf16 v[34:49], v[178:181], v[174:177], v[34:49]
	v_mfma_f32_32x32x16_bf16 v[50:65], v[166:169], v[170:173], v[50:65]
	v_mfma_f32_32x32x16_bf16 v[34:49], v[162:165], v[170:173], v[34:49]
	v_sub_f32_e32 v212, v116, v212
	v_sub_f32_e32 v213, v116, v213
	v_sub_f32_e32 v214, v116, v214
	v_sub_f32_e32 v215, v116, v215
	v_sub_f32_e32 v216, v116, v216
	v_sub_f32_e32 v217, v116, v217
	v_sub_f32_e32 v218, v116, v218
	v_sub_f32_e32 v219, v116, v219
	v_sub_f32_e32 v220, v116, v220
	v_sub_f32_e32 v221, v116, v221
	v_sub_f32_e32 v222, v116, v222
	v_sub_f32_e32 v223, v116, v223
	v_sub_f32_e32 v224, v116, v224
	v_sub_f32_e32 v225, v116, v225
	v_sub_f32_e32 v226, v116, v226
	v_sub_f32_e32 v227, v116, v227
	v_mul_f32_e32 v212, 0x3fb8aa3b, v212
	v_mul_f32_e32 v213, 0x3fb8aa3b, v213
	v_mul_f32_e32 v214, 0x3fb8aa3b, v214
	v_mul_f32_e32 v215, 0x3fb8aa3b, v215
	v_mul_f32_e32 v216, 0x3fb8aa3b, v216
	v_mul_f32_e32 v217, 0x3fb8aa3b, v217
	v_mul_f32_e32 v218, 0x3fb8aa3b, v218
	v_mul_f32_e32 v219, 0x3fb8aa3b, v219
	v_mul_f32_e32 v220, 0x3fb8aa3b, v220
	v_mul_f32_e32 v221, 0x3fb8aa3b, v221
	v_mul_f32_e32 v222, 0x3fb8aa3b, v222
	v_mul_f32_e32 v223, 0x3fb8aa3b, v223
	v_mul_f32_e32 v224, 0x3fb8aa3b, v224
	v_mul_f32_e32 v225, 0x3fb8aa3b, v225
	v_mul_f32_e32 v226, 0x3fb8aa3b, v226
	v_mul_f32_e32 v227, 0x3fb8aa3b, v227
	v_exp_f32_e32 v212, v212
	v_exp_f32_e32 v213, v213
	v_exp_f32_e32 v214, v214
	v_exp_f32_e32 v215, v215
	v_exp_f32_e32 v216, v216
	v_exp_f32_e32 v217, v217
	v_exp_f32_e32 v218, v218
	v_exp_f32_e32 v219, v219
	v_exp_f32_e32 v220, v220
	v_exp_f32_e32 v221, v221
	v_exp_f32_e32 v222, v222
	v_exp_f32_e32 v223, v223
	v_exp_f32_e32 v224, v224
	v_exp_f32_e32 v225, v225
	v_exp_f32_e32 v226, v226
	v_exp_f32_e32 v227, v227
	v_mul_f32_e32 v212, v66, v212
	v_mul_f32_e32 v213, v67, v213
	v_mul_f32_e32 v214, v68, v214
	v_mul_f32_e32 v215, v69, v215
	v_mul_f32_e32 v216, v70, v216
	v_mul_f32_e32 v217, v71, v217
	v_mul_f32_e32 v218, v72, v218
	v_mul_f32_e32 v219, v73, v219
	v_mul_f32_e32 v220, v74, v220
	v_mul_f32_e32 v221, v75, v221
	v_mul_f32_e32 v222, v76, v222
	v_mul_f32_e32 v223, v77, v223
	v_mul_f32_e32 v224, v78, v224
	v_mul_f32_e32 v225, v79, v225
	v_mul_f32_e32 v226, v80, v226
	v_mul_f32_e32 v227, v81, v227
	v_cndmask_b32_e64 v153, 0, v212, vcc
	v_cndmask_b32_e64 v157, 0, v213, s[38:39]
	v_cndmask_b32_e64 v66, 0, v214, s[40:41]
	v_cndmask_b32_e64 v68, 0, v215, s[42:43]
	v_cndmask_b32_e64 v67, 0, v216, s[44:45]
	v_cndmask_b32_e64 v70, 0, v217, s[46:47]
	v_cndmask_b32_e64 v69, 0, v218, s[48:49]
	v_cndmask_b32_e64 v72, 0, v219, s[50:51]
	v_cndmask_b32_e64 v71, 0, v220, s[52:53]
	v_cndmask_b32_e64 v74, 0, v221, s[54:55]
	v_cndmask_b32_e64 v73, 0, v222, s[56:57]
	v_cndmask_b32_e64 v76, 0, v223, s[58:59]
	v_cndmask_b32_e64 v75, 0, v224, s[60:61]
	v_cndmask_b32_e64 v78, 0, v225, s[62:63]
	v_cndmask_b32_e64 v77, 0, v226, s[64:65]
	v_cndmask_b32_e64 v79, 0, v227, s[66:67]
	s_branch .LBB0_587
